# HGRN chunk loop (Lever 1): the full VMEM drain before step C becomes vmcnt(6) (only the gate prefetch of chunk 0 must have landed; the next chunk's f/q/v prefetches stay in flight); on top of the rec_
# speedup vs baseline: 1.0110x; 1.0040x over previous
.LBB0_664:
	s_nop 7
	v_cndmask_b32_e64 v66, v66, 0, s[18:19]
	v_bfe_u32 v70, v66, 16, 1
	v_add3_u32 v66, v66, v70, s48
	ds_write_b16_d16_hi v156, v66
	v_cndmask_b32_e64 v66, v67, 0, s[20:21]
	v_bfe_u32 v67, v66, 16, 1
	v_add3_u32 v66, v66, v67, s48
	ds_write_b16_d16_hi v156, v66 offset:144
	v_cndmask_b32_e64 v66, v68, 0, s[22:23]
	v_bfe_u32 v67, v66, 16, 1
	v_add3_u32 v66, v66, v67, s48
	ds_write_b16_d16_hi v156, v66 offset:288
	v_cndmask_b32_e64 v66, v69, 0, s[24:25]
	v_bfe_u32 v67, v66, 16, 1
	v_add3_u32 v66, v66, v67, s48
	ds_write_b16_d16_hi v156, v66 offset:432
	s_waitcnt lgkmcnt(0)
	s_barrier
	s_waitcnt vmcnt(6)
	v_mov_b64_e32 v[68:69], v[48:49]
	v_mov_b64_e32 v[72:73], v[40:41]
	s_and_b64 vcc, exec, s[26:27]
	v_mov_b64_e32 v[66:67], v[46:47]
	v_mov_b64_e32 v[70:71], v[38:39]
	s_cbranch_vccnz .LBB0_666
	v_mov_b32_e32 v66, v126
	v_mov_b32_e32 v67, v125
	v_mov_b32_e32 v108, v127
	s_add_u32 s26, s50, s38
	s_addc_u32 s27, s51, s39
	v_lshl_add_u64 v[66:67], s[26:27], 0, v[108:109]
	s_mov_b64 s[26:27], 0x26240000
	v_lshl_add_u64 v[70:71], v[66:67], 0, s[26:27]
	v_add_co_u32_e32 v66, vcc, 0x26240000, v66
	s_nop 1
	v_addc_co_u32_e32 v67, vcc, 0, v67, vcc
	global_load_dwordx4 v[66:69], v[66:67], off nt
	s_nop 0
	global_load_dwordx4 v[70:73], v[70:71], off offset:16 nt
